# barrier acquire in two levels: the XCD leader invalidates the L2 once (buffer_inv sc1) after the grid-wide poll and then releases its XCD; other workgroups invalidate only their L1 (formally agent-sco
# speedup vs baseline: 1.0139x; 1.0139x over previous
; template <class T> __device__ __forceinline__ T* opaque_p(T* p) { asm volatile("" : "+s"(p)); return p; }
; __device__ __forceinline__ int tidx(int wid) { int l; asm volatile("v_mbcnt_lo_u32_b32 %0, -1, 0\n\tv_mbcnt_hi_u32_b32 %0, -1, %0" : "=v"(l)); return (wid << 6) + l; }
; __device__ __forceinline__ unsigned xb_ld(unsigned* p)              { return __hip_atomic_load(p, __ATOMIC_RELAXED, __HIP_MEMORY_SCOPE_AGENT); }
; __device__ __forceinline__ unsigned xb_add(unsigned* p, unsigned v) { return __hip_atomic_fetch_add(p, v, __ATOMIC_RELAXED, __HIP_MEMORY_SCOPE_AGENT); }
; #define XB_SPIN(cond, bar) do { unsigned _sp = 0; while (cond) { __builtin_amdgcn_s_sleep(1); \
;     if ((++_sp & 255u) == 0u) { if (xb_ld(&(bar)[XB_TMO])) break; if (_sp > XB_SPIN_CAP) { atomicAdd(&(bar)[XB_TMO], 1u); break; } } } } while (0)
; __device__ __forceinline__ void xcd_barrier(const XcdBarrier& b, int wid0) {
;     asm volatile("s_waitcnt vmcnt(0)" ::: "memory");
;     __syncthreads();
;     if (tidx(wid0) == 0) {
;         unsigned* bar = opaque_p(b.bar);
;         __builtin_amdgcn_s_waitcnt(0);
;         unsigned nloc = b.st[0], nx = b.st[1];
;         if (nloc == 0u) { xcd_barrier_complete(bar, b.x, nloc, nx); b.st[0] = nloc; b.st[1] = nx; }
;         const unsigned old = xb_add(&bar[XB_XSUB(b.x)], 1u);
;         const unsigned gen = old / nloc;
;         if (old + 1u == (gen + 1u) * nloc) {
;             __builtin_amdgcn_fence(__ATOMIC_RELEASE, "agent");
;             asm volatile("s_waitcnt vmcnt(0)" ::: "memory");
;             const unsigned og = xb_add(&bar[XB_TOP], 1u);
;             const unsigned tg = og / nx;
;             if (og + 1u == (tg + 1u) * nx) xb_add(&bar[XB_TOPGEN], 1u);
;             else XB_SPIN(xb_ld(&bar[XB_TOPGEN]) == tg, bar);
;             (void)xb_add(&bar[XB_XGEN(b.x)], 1u);
;             __builtin_amdgcn_fence(__ATOMIC_ACQUIRE, "agent");
;             asm volatile("s_waitcnt vmcnt(0)" ::: "memory");
;         } else {
;             XB_SPIN(xb_ld(&bar[XB_XGEN(b.x)]) == gen, bar);
;             __builtin_amdgcn_fence(__ATOMIC_ACQUIRE, "agent");
;             asm volatile("s_waitcnt vmcnt(0)" ::: "memory");
;         }
;     }
;     __syncthreads();
; }
.LBB0_284:
	s_or_b32 s36, s77, 2
	s_cmp_ge_i32 s36, s61
	s_cbranch_scc1 .LBB0_330
	s_waitcnt vmcnt(0)
	s_waitcnt vmcnt(0) lgkmcnt(0)
	s_barrier
	v_mbcnt_lo_u32_b32 v0, -1, 0
	v_mbcnt_hi_u32_b32 v0, -1, v0
	s_nop 0
	v_cmp_eq_u32_e32 vcc, s86, v0
	s_and_saveexec_b64 s[30:31], vcc
	s_cbranch_execz .LBB0_329
	v_readlane_b32 s34, v255, 3
	v_readlane_b32 s0, v255, 17
	v_readlane_b32 s35, v255, 4
	v_readlane_b32 s1, v255, 18
	s_lshl_b32 s2, s91, 2
	s_add_u32 s2, s34, s2
	s_addc_u32 s3, s35, 0
	s_add_u32 s4, s2, 0x1400
	s_addc_u32 s5, s3, 0
	s_add_u32 s6, s34, 0x3400
	s_addc_u32 s7, s35, 0
	v_mov_b32_e32 v0, s0
	v_mov_b32_e32 v1, s1
	ds_read_b32 v2, v0
	ds_read_b32 v12, v1
	v_mov_b32_e32 v6, 1
	v_mov_b32_e32 v8, s4
	v_mov_b32_e32 v9, s5
	s_add_u32 s10, s2, 0x2400
	s_addc_u32 s11, s3, 0
	v_mov_b32_e32 v16, s10
	v_mov_b32_e32 v17, s11
	v_mov_b32_e32 v10, s6
	v_mov_b32_e32 v11, s7
	s_nop 0
	global_atomic_add v3, v[8:9], v6, off sc0
	s_waitcnt lgkmcnt(0)
	v_cvt_f32_u32_e32 v1, v2
	v_sub_u32_e32 v4, 0, v2
	v_rcp_iflag_f32_e32 v1, v1
	s_nop 0
	v_mul_f32_e32 v1, 0x4f7ffffe, v1
	v_cvt_u32_f32_e32 v1, v1
	v_mul_lo_u32 v4, v4, v1
	v_mul_hi_u32 v4, v1, v4
	v_add_u32_e32 v1, v1, v4
	s_mov_b32 s8, 0
	s_waitcnt vmcnt(0)
	v_mul_hi_u32 v1, v3, v1
	v_mul_lo_u32 v4, v1, v2
	v_sub_u32_e32 v4, v3, v4
	v_cmp_ge_u32_e32 vcc, v4, v2
	v_add_u32_e32 v5, 1, v1
	s_nop 1
	v_cndmask_b32_e32 v1, v1, v5, vcc
	v_sub_u32_e32 v5, v4, v2
	v_cndmask_b32_e32 v4, v4, v5, vcc
	v_cmp_ge_u32_e32 vcc, v4, v2
	v_add_u32_e32 v4, 1, v1
	s_nop 1
	v_cndmask_b32_e32 v1, v1, v4, vcc
	v_add_u32_e32 v1, 1, v1
	v_add_u32_e32 v4, 1, v3
	v_mul_lo_u32 v7, v1, v2
	v_mul_lo_u32 v13, v1, v12
	v_cmp_ne_u32_e32 vcc, v4, v7
	s_nop 1
	s_cbranch_vccnz .Lxb0_wait
	buffer_wbl2 sc1
	s_waitcnt vmcnt(0)
	global_atomic_add v[10:11], v6, off

; __device__ __forceinline__ unsigned xb_ld(unsigned* p)              { return __hip_atomic_load(p, __ATOMIC_RELAXED, __HIP_MEMORY_SCOPE_AGENT); }
; __device__ __forceinline__ unsigned xb_add(unsigned* p, unsigned v) { return __hip_atomic_fetch_add(p, v, __ATOMIC_RELAXED, __HIP_MEMORY_SCOPE_AGENT); }
; #define XB_SPIN(cond, bar) do { unsigned _sp = 0; while (cond) { __builtin_amdgcn_s_sleep(1); \
;     if ((++_sp & 255u) == 0u) { if (xb_ld(&(bar)[XB_TMO])) break; if (_sp > XB_SPIN_CAP) { atomicAdd(&(bar)[XB_TMO], 1u); break; } } } } while (0)
; __device__ __forceinline__ void xcd_barrier(const XcdBarrier& b, int wid0) {
;     ...
;         const unsigned old = xb_add(&bar[XB_XSUB(b.x)], 1u);
;         const unsigned gen = old / nloc;
;         if (old + 1u == (gen + 1u) * nloc) {
;             __builtin_amdgcn_fence(__ATOMIC_RELEASE, "agent");
;             asm volatile("s_waitcnt vmcnt(0)" ::: "memory");
;             const unsigned og = xb_add(&bar[XB_TOP], 1u);
;             const unsigned tg = og / nx;
;             if (og + 1u == (tg + 1u) * nx) xb_add(&bar[XB_TOPGEN], 1u);
;             else XB_SPIN(xb_ld(&bar[XB_TOPGEN]) == tg, bar);
;             (void)xb_add(&bar[XB_XGEN(b.x)], 1u);
;             __builtin_amdgcn_fence(__ATOMIC_ACQUIRE, "agent");
;             asm volatile("s_waitcnt vmcnt(0)" ::: "memory");
;         } else {
;             XB_SPIN(xb_ld(&bar[XB_XGEN(b.x)]) == gen, bar);
;             __builtin_amdgcn_fence(__ATOMIC_ACQUIRE, "agent");
;             asm volatile("s_waitcnt vmcnt(0)" ::: "memory");
;         }
.Lxb0_ldone:
	buffer_inv sc1
	s_waitcnt vmcnt(0)
	global_atomic_add v[16:17], v6, off
	s_branch .Lxb0_done
.Lxb0_wait:
	global_load_dword v14, v[16:17], off sc1
	s_add_i32 s8, s8, 1
	s_waitcnt vmcnt(0)
	v_cmp_lt_u32_e32 vcc, v14, v1
	s_nop 1
	s_cbranch_vccz .Lxb0_wdone
	s_cmp_lt_u32 s8, 0x40000
	s_cbranch_scc0 .Lxb0_wdone
	s_sleep 1
	s_branch .Lxb0_wait

; __device__ __forceinline__ unsigned xb_ld(unsigned* p)              { return __hip_atomic_load(p, __ATOMIC_RELAXED, __HIP_MEMORY_SCOPE_AGENT); }
; #define XB_SPIN(cond, bar) do { unsigned _sp = 0; while (cond) { __builtin_amdgcn_s_sleep(1); \
;     if ((++_sp & 255u) == 0u) { if (xb_ld(&(bar)[XB_TMO])) break; if (_sp > XB_SPIN_CAP) { atomicAdd(&(bar)[XB_TMO], 1u); break; } } } } while (0)
; __device__ __forceinline__ void xcd_barrier(const XcdBarrier& b, int wid0) {
;     ...
;             XB_SPIN(xb_ld(&bar[XB_XGEN(b.x)]) == gen, bar);
;             __builtin_amdgcn_fence(__ATOMIC_ACQUIRE, "agent");
;             asm volatile("s_waitcnt vmcnt(0)" ::: "memory");
;         }
;     }
;     __syncthreads();
.Lxb0_done:
.LBB0_329:
	s_or_b64 exec, exec, s[30:31]
	s_barrier

; template <class T> __device__ __forceinline__ T* opaque_p(T* p) { asm volatile("" : "+s"(p)); return p; }
; __device__ __forceinline__ int tidx(int wid) { int l; asm volatile("v_mbcnt_lo_u32_b32 %0, -1, 0\n\tv_mbcnt_hi_u32_b32 %0, -1, %0" : "=v"(l)); return (wid << 6) + l; }
; __device__ __forceinline__ unsigned xb_add(unsigned* p, unsigned v) { return __hip_atomic_fetch_add(p, v, __ATOMIC_RELAXED, __HIP_MEMORY_SCOPE_AGENT); }
; __device__ __forceinline__ void xcd_barrier(const XcdBarrier& b, int wid0) {
;     asm volatile("s_waitcnt vmcnt(0)" ::: "memory");
;     __syncthreads();
;     if (tidx(wid0) == 0) {
;         unsigned* bar = opaque_p(b.bar);
;         __builtin_amdgcn_s_waitcnt(0);
;         unsigned nloc = b.st[0], nx = b.st[1];
;         if (nloc == 0u) { xcd_barrier_complete(bar, b.x, nloc, nx); b.st[0] = nloc; b.st[1] = nx; }
;         const unsigned old = xb_add(&bar[XB_XSUB(b.x)], 1u);
;         const unsigned gen = old / nloc;
;         if (old + 1u == (gen + 1u) * nloc) {
;             __builtin_amdgcn_fence(__ATOMIC_RELEASE, "agent");
;             asm volatile("s_waitcnt vmcnt(0)" ::: "memory");
;             const unsigned og = xb_add(&bar[XB_TOP], 1u);
;             const unsigned tg = og / nx;
;             if (og + 1u == (tg + 1u) * nx) xb_add(&bar[XB_TOPGEN], 1u);
.LBB0_521:
	s_or_b32 s36, s77, 3
	s_cmp_lt_i32 s36, s61
	s_cbranch_scc0 .LBB0_567
	s_waitcnt vmcnt(0)
	s_barrier
	v_mbcnt_lo_u32_b32 v0, -1, 0
	v_mbcnt_hi_u32_b32 v0, -1, v0
	s_nop 0
	v_cmp_eq_u32_e32 vcc, s86, v0
	s_and_saveexec_b64 s[30:31], vcc
	s_cbranch_execz .LBB0_566
	v_readlane_b32 s34, v255, 3
	v_readlane_b32 s0, v255, 17
	v_readlane_b32 s35, v255, 4
	v_readlane_b32 s1, v255, 18
	s_lshl_b32 s2, s91, 2
	s_add_u32 s2, s34, s2
	s_addc_u32 s3, s35, 0
	s_add_u32 s4, s2, 0x1400
	s_addc_u32 s5, s3, 0
	s_add_u32 s6, s34, 0x3400
	s_addc_u32 s7, s35, 0
	v_mov_b32_e32 v0, s0
	v_mov_b32_e32 v1, s1
	ds_read_b32 v2, v0
	ds_read_b32 v12, v1
	v_mov_b32_e32 v6, 1
	v_mov_b32_e32 v8, s4
	v_mov_b32_e32 v9, s5
	s_add_u32 s10, s2, 0x2400
	s_addc_u32 s11, s3, 0
	v_mov_b32_e32 v16, s10
	v_mov_b32_e32 v17, s11
	v_mov_b32_e32 v10, s6
	v_mov_b32_e32 v11, s7
	s_nop 0
	global_atomic_add v3, v[8:9], v6, off sc0
	s_waitcnt lgkmcnt(0)
	v_cvt_f32_u32_e32 v1, v2
	v_sub_u32_e32 v4, 0, v2
	v_rcp_iflag_f32_e32 v1, v1
	s_nop 0
	v_mul_f32_e32 v1, 0x4f7ffffe, v1
	v_cvt_u32_f32_e32 v1, v1
	v_mul_lo_u32 v4, v4, v1
	v_mul_hi_u32 v4, v1, v4
	v_add_u32_e32 v1, v1, v4
	s_mov_b32 s8, 0
	s_waitcnt vmcnt(0)
	v_mul_hi_u32 v1, v3, v1
	v_mul_lo_u32 v4, v1, v2
	v_sub_u32_e32 v4, v3, v4
	v_cmp_ge_u32_e32 vcc, v4, v2
	v_add_u32_e32 v5, 1, v1
	s_nop 1
	v_cndmask_b32_e32 v1, v1, v5, vcc
	v_sub_u32_e32 v5, v4, v2
	v_cndmask_b32_e32 v4, v4, v5, vcc
	v_cmp_ge_u32_e32 vcc, v4, v2
	v_add_u32_e32 v4, 1, v1
	s_nop 1
	v_cndmask_b32_e32 v1, v1, v4, vcc
	v_add_u32_e32 v1, 1, v1
	v_add_u32_e32 v4, 1, v3
	v_mul_lo_u32 v7, v1, v2
	v_mul_lo_u32 v13, v1, v12
	v_cmp_ne_u32_e32 vcc, v4, v7
	s_nop 1
	s_cbranch_vccnz .Lxb1_wait
	buffer_wbl2 sc1
	s_waitcnt vmcnt(0)
	global_atomic_add v[10:11], v6, off

; template <class T> __device__ __forceinline__ T* opaque_p(T* p) { asm volatile("" : "+s"(p)); return p; }
; __device__ __forceinline__ int tidx(int wid) { int l; asm volatile("v_mbcnt_lo_u32_b32 %0, -1, 0\n\tv_mbcnt_hi_u32_b32 %0, -1, %0" : "=v"(l)); return (wid << 6) + l; }
; __device__ __forceinline__ unsigned xb_add(unsigned* p, unsigned v) { return __hip_atomic_fetch_add(p, v, __ATOMIC_RELAXED, __HIP_MEMORY_SCOPE_AGENT); }
; __device__ __forceinline__ void xcd_barrier(const XcdBarrier& b, int wid0) {
;     asm volatile("s_waitcnt vmcnt(0)" ::: "memory");
;     __syncthreads();
;     if (tidx(wid0) == 0) {
;         unsigned* bar = opaque_p(b.bar);
;         __builtin_amdgcn_s_waitcnt(0);
;         unsigned nloc = b.st[0], nx = b.st[1];
;         if (nloc == 0u) { xcd_barrier_complete(bar, b.x, nloc, nx); b.st[0] = nloc; b.st[1] = nx; }
;         const unsigned old = xb_add(&bar[XB_XSUB(b.x)], 1u);
;         const unsigned gen = old / nloc;
;         if (old + 1u == (gen + 1u) * nloc) {
;             __builtin_amdgcn_fence(__ATOMIC_RELEASE, "agent");
;             asm volatile("s_waitcnt vmcnt(0)" ::: "memory");
;             const unsigned og = xb_add(&bar[XB_TOP], 1u);
;             const unsigned tg = og / nx;
;             if (og + 1u == (tg + 1u) * nx) xb_add(&bar[XB_TOPGEN], 1u);
.LBB0_698:
	s_add_i32 s0, s77, 4
	s_cmp_ge_i32 s0, s61
	s_cbranch_scc1 .LBB0_744
	s_waitcnt vmcnt(0)
	s_waitcnt vmcnt(0) lgkmcnt(0)
	s_barrier
	v_mbcnt_lo_u32_b32 v0, -1, 0
	v_mbcnt_hi_u32_b32 v0, -1, v0
	s_nop 0
	v_cmp_eq_u32_e32 vcc, s86, v0
	s_and_saveexec_b64 s[30:31], vcc
	s_cbranch_execz .LBB0_743
	v_readlane_b32 s34, v255, 3
	v_readlane_b32 s0, v255, 17
	v_readlane_b32 s35, v255, 4
	v_readlane_b32 s1, v255, 18
	s_lshl_b32 s2, s91, 2
	s_add_u32 s2, s34, s2
	s_addc_u32 s3, s35, 0
	s_add_u32 s4, s2, 0x1400
	s_addc_u32 s5, s3, 0
	s_add_u32 s6, s34, 0x3400
	s_addc_u32 s7, s35, 0
	v_mov_b32_e32 v0, s0
	v_mov_b32_e32 v1, s1
	ds_read_b32 v2, v0
	ds_read_b32 v12, v1
	v_mov_b32_e32 v6, 1
	v_mov_b32_e32 v8, s4
	v_mov_b32_e32 v9, s5
	s_add_u32 s10, s2, 0x2400
	s_addc_u32 s11, s3, 0
	v_mov_b32_e32 v16, s10
	v_mov_b32_e32 v17, s11
	v_mov_b32_e32 v10, s6
	v_mov_b32_e32 v11, s7
	s_nop 0
	global_atomic_add v3, v[8:9], v6, off sc0
	s_waitcnt lgkmcnt(0)
	v_cvt_f32_u32_e32 v1, v2
	v_sub_u32_e32 v4, 0, v2
	v_rcp_iflag_f32_e32 v1, v1
	s_nop 0
	v_mul_f32_e32 v1, 0x4f7ffffe, v1
	v_cvt_u32_f32_e32 v1, v1
	v_mul_lo_u32 v4, v4, v1
	v_mul_hi_u32 v4, v1, v4
	v_add_u32_e32 v1, v1, v4
	s_mov_b32 s8, 0
	s_waitcnt vmcnt(0)
	v_mul_hi_u32 v1, v3, v1
	v_mul_lo_u32 v4, v1, v2
	v_sub_u32_e32 v4, v3, v4
	v_cmp_ge_u32_e32 vcc, v4, v2
	v_add_u32_e32 v5, 1, v1
	s_nop 1
	v_cndmask_b32_e32 v1, v1, v5, vcc
	v_sub_u32_e32 v5, v4, v2
	v_cndmask_b32_e32 v4, v4, v5, vcc
	v_cmp_ge_u32_e32 vcc, v4, v2
	v_add_u32_e32 v4, 1, v1
	s_nop 1
	v_cndmask_b32_e32 v1, v1, v4, vcc
	v_add_u32_e32 v1, 1, v1
	v_add_u32_e32 v4, 1, v3
	v_mul_lo_u32 v7, v1, v2
	v_mul_lo_u32 v13, v1, v12
	v_cmp_ne_u32_e32 vcc, v4, v7
	s_nop 1
	s_cbranch_vccnz .Lxb2_wait
	buffer_wbl2 sc1
	s_waitcnt vmcnt(0)
	global_atomic_add v[10:11], v6, off

; template <class T> __device__ __forceinline__ T* opaque_p(T* p) { asm volatile("" : "+s"(p)); return p; }
; __device__ __forceinline__ int tidx(int wid) { int l; asm volatile("v_mbcnt_lo_u32_b32 %0, -1, 0\n\tv_mbcnt_hi_u32_b32 %0, -1, %0" : "=v"(l)); return (wid << 6) + l; }
; __device__ __forceinline__ unsigned xb_add(unsigned* p, unsigned v) { return __hip_atomic_fetch_add(p, v, __ATOMIC_RELAXED, __HIP_MEMORY_SCOPE_AGENT); }
; __device__ __forceinline__ void xcd_barrier(const XcdBarrier& b, int wid0) {
;     asm volatile("s_waitcnt vmcnt(0)" ::: "memory");
;     __syncthreads();
;     if (tidx(wid0) == 0) {
;         unsigned* bar = opaque_p(b.bar);
;         __builtin_amdgcn_s_waitcnt(0);
;         unsigned nloc = b.st[0], nx = b.st[1];
;         if (nloc == 0u) { xcd_barrier_complete(bar, b.x, nloc, nx); b.st[0] = nloc; b.st[1] = nx; }
;         const unsigned old = xb_add(&bar[XB_XSUB(b.x)], 1u);
;         const unsigned gen = old / nloc;
;         if (old + 1u == (gen + 1u) * nloc) {
;             __builtin_amdgcn_fence(__ATOMIC_RELEASE, "agent");
;             asm volatile("s_waitcnt vmcnt(0)" ::: "memory");
;             const unsigned og = xb_add(&bar[XB_TOP], 1u);
;             const unsigned tg = og / nx;
;             if (og + 1u == (tg + 1u) * nx) xb_add(&bar[XB_TOPGEN], 1u);
.LBB0_759:
	v_readlane_b32 s0, v255, 33
	s_add_i32 s36, s77, 6
	v_readlane_b32 s1, v255, 34
	s_cmp_lt_i32 s36, s1
	s_cbranch_scc0 .LBB0_772
	s_waitcnt vmcnt(0)
	s_waitcnt lgkmcnt(0)
	s_barrier
	v_mbcnt_lo_u32_b32 v0, -1, 0
	v_mbcnt_hi_u32_b32 v0, -1, v0
	s_nop 0
	v_cmp_eq_u32_e32 vcc, s86, v0
	s_and_saveexec_b64 s[30:31], vcc
	s_mov_b32 s93, s61
	v_readlane_b32 s96, v255, 28
	v_readlane_b32 s60, v255, 33
	v_readlane_b32 s97, v255, 29
	v_readlane_b32 s94, v255, 32
	v_readlane_b32 s61, v255, 34
	s_cbranch_execz .LBB0_805
	v_readlane_b32 s34, v255, 3
	v_readlane_b32 s0, v255, 17
	v_readlane_b32 s35, v255, 4
	v_readlane_b32 s1, v255, 18
	s_lshl_b32 s2, s91, 2
	s_add_u32 s2, s34, s2
	s_addc_u32 s3, s35, 0
	s_add_u32 s4, s2, 0x1400
	s_addc_u32 s5, s3, 0
	s_add_u32 s6, s34, 0x3400
	s_addc_u32 s7, s35, 0
	v_mov_b32_e32 v0, s0
	v_mov_b32_e32 v1, s1
	ds_read_b32 v2, v0
	ds_read_b32 v12, v1
	v_mov_b32_e32 v6, 1
	v_mov_b32_e32 v8, s4
	v_mov_b32_e32 v9, s5
	s_add_u32 s10, s2, 0x2400
	s_addc_u32 s11, s3, 0
	v_mov_b32_e32 v16, s10
	v_mov_b32_e32 v17, s11
	v_mov_b32_e32 v10, s6
	v_mov_b32_e32 v11, s7
	s_nop 0
	global_atomic_add v3, v[8:9], v6, off sc0
	s_waitcnt lgkmcnt(0)
	v_cvt_f32_u32_e32 v1, v2
	v_sub_u32_e32 v4, 0, v2
	v_rcp_iflag_f32_e32 v1, v1
	s_nop 0
	v_mul_f32_e32 v1, 0x4f7ffffe, v1
	v_cvt_u32_f32_e32 v1, v1
	v_mul_lo_u32 v4, v4, v1
	v_mul_hi_u32 v4, v1, v4
	v_add_u32_e32 v1, v1, v4
	s_mov_b32 s8, 0
	s_waitcnt vmcnt(0)
	v_mul_hi_u32 v1, v3, v1
	v_mul_lo_u32 v4, v1, v2
	v_sub_u32_e32 v4, v3, v4
	v_cmp_ge_u32_e32 vcc, v4, v2
	v_add_u32_e32 v5, 1, v1
	s_nop 1
	v_cndmask_b32_e32 v1, v1, v5, vcc
	v_sub_u32_e32 v5, v4, v2
	v_cndmask_b32_e32 v4, v4, v5, vcc
	v_cmp_ge_u32_e32 vcc, v4, v2
	v_add_u32_e32 v4, 1, v1
	s_nop 1
	v_cndmask_b32_e32 v1, v1, v4, vcc
	v_add_u32_e32 v1, 1, v1
	v_add_u32_e32 v4, 1, v3
	v_mul_lo_u32 v7, v1, v2
	v_mul_lo_u32 v13, v1, v12
	v_cmp_ne_u32_e32 vcc, v4, v7
	s_nop 1
	s_cbranch_vccnz .Lxb3_wait
	buffer_wbl2 sc1
	s_waitcnt vmcnt(0)
	global_atomic_add v[10:11], v6, off

; __device__ __forceinline__ unsigned xb_ld(unsigned* p)              { return __hip_atomic_load(p, __ATOMIC_RELAXED, __HIP_MEMORY_SCOPE_AGENT); }
; #define XB_SPIN(cond, bar) do { unsigned _sp = 0; while (cond) { __builtin_amdgcn_s_sleep(1); \
;     if ((++_sp & 255u) == 0u) { if (xb_ld(&(bar)[XB_TMO])) break; if (_sp > XB_SPIN_CAP) { atomicAdd(&(bar)[XB_TMO], 1u); break; } } } } while (0)
; __device__ __forceinline__ void xcd_barrier(const XcdBarrier& b, int wid0) {
;     ...
;             XB_SPIN(xb_ld(&bar[XB_XGEN(b.x)]) == gen, bar);
;             __builtin_amdgcn_fence(__ATOMIC_ACQUIRE, "agent");
;             asm volatile("s_waitcnt vmcnt(0)" ::: "memory");
;         }
;     }
;     __syncthreads();
.Lxb3_done:
	s_branch .LBB0_805
.LBB0_772:
	s_mov_b32 s93, s61
	v_readlane_b32 s96, v255, 28
	v_readlane_b32 s60, v255, 33
	v_readlane_b32 s97, v255, 29
	v_readlane_b32 s94, v255, 32
	v_readlane_b32 s61, v255, 34
	s_branch .LBB0_806

; template <class T> __device__ __forceinline__ T* opaque_p(T* p) { asm volatile("" : "+s"(p)); return p; }
; __device__ __forceinline__ int tidx(int wid) { int l; asm volatile("v_mbcnt_lo_u32_b32 %0, -1, 0\n\tv_mbcnt_hi_u32_b32 %0, -1, %0" : "=v"(l)); return (wid << 6) + l; }
; __device__ __forceinline__ unsigned xb_add(unsigned* p, unsigned v) { return __hip_atomic_fetch_add(p, v, __ATOMIC_RELAXED, __HIP_MEMORY_SCOPE_AGENT); }
; __device__ __forceinline__ void xcd_barrier(const XcdBarrier& b, int wid0) {
;     asm volatile("s_waitcnt vmcnt(0)" ::: "memory");
;     __syncthreads();
;     if (tidx(wid0) == 0) {
;         unsigned* bar = opaque_p(b.bar);
;         __builtin_amdgcn_s_waitcnt(0);
;         unsigned nloc = b.st[0], nx = b.st[1];
;         if (nloc == 0u) { xcd_barrier_complete(bar, b.x, nloc, nx); b.st[0] = nloc; b.st[1] = nx; }
;         const unsigned old = xb_add(&bar[XB_XSUB(b.x)], 1u);
;         const unsigned gen = old / nloc;
;         if (old + 1u == (gen + 1u) * nloc) {
;             __builtin_amdgcn_fence(__ATOMIC_RELEASE, "agent");
;             asm volatile("s_waitcnt vmcnt(0)" ::: "memory");
;             const unsigned og = xb_add(&bar[XB_TOP], 1u);
;             const unsigned tg = og / nx;
;             if (og + 1u == (tg + 1u) * nx) xb_add(&bar[XB_TOPGEN], 1u);
.LBB0_835:
	s_add_i32 s36, s77, 7
	s_cmp_ge_i32 s36, s61
	s_cbranch_scc1 .LBB0_881
	s_waitcnt vmcnt(0)
	s_waitcnt lgkmcnt(0)
	s_barrier
	v_mbcnt_lo_u32_b32 v0, -1, 0
	v_mbcnt_hi_u32_b32 v0, -1, v0
	s_nop 0
	v_cmp_eq_u32_e32 vcc, s86, v0
	s_and_saveexec_b64 s[30:31], vcc
	s_cbranch_execz .LBB0_880
	v_readlane_b32 s34, v255, 3
	v_readlane_b32 s0, v255, 17
	v_readlane_b32 s35, v255, 4
	v_readlane_b32 s1, v255, 18
	s_lshl_b32 s2, s91, 2
	s_add_u32 s2, s34, s2
	s_addc_u32 s3, s35, 0
	s_add_u32 s4, s2, 0x1400
	s_addc_u32 s5, s3, 0
	s_add_u32 s6, s34, 0x3400
	s_addc_u32 s7, s35, 0
	v_mov_b32_e32 v0, s0
	v_mov_b32_e32 v1, s1
	ds_read_b32 v2, v0
	ds_read_b32 v12, v1
	v_mov_b32_e32 v6, 1
	v_mov_b32_e32 v8, s4
	v_mov_b32_e32 v9, s5
	s_add_u32 s10, s2, 0x2400
	s_addc_u32 s11, s3, 0
	v_mov_b32_e32 v16, s10
	v_mov_b32_e32 v17, s11
	v_mov_b32_e32 v10, s6
	v_mov_b32_e32 v11, s7
	s_nop 0
	global_atomic_add v3, v[8:9], v6, off sc0
	s_waitcnt lgkmcnt(0)
	v_cvt_f32_u32_e32 v1, v2
	v_sub_u32_e32 v4, 0, v2
	v_rcp_iflag_f32_e32 v1, v1
	s_nop 0
	v_mul_f32_e32 v1, 0x4f7ffffe, v1
	v_cvt_u32_f32_e32 v1, v1
	v_mul_lo_u32 v4, v4, v1
	v_mul_hi_u32 v4, v1, v4
	v_add_u32_e32 v1, v1, v4
	s_mov_b32 s8, 0
	s_waitcnt vmcnt(0)
	v_mul_hi_u32 v1, v3, v1
	v_mul_lo_u32 v4, v1, v2
	v_sub_u32_e32 v4, v3, v4
	v_cmp_ge_u32_e32 vcc, v4, v2
	v_add_u32_e32 v5, 1, v1
	s_nop 1
	v_cndmask_b32_e32 v1, v1, v5, vcc
	v_sub_u32_e32 v5, v4, v2
	v_cndmask_b32_e32 v4, v4, v5, vcc
	v_cmp_ge_u32_e32 vcc, v4, v2
	v_add_u32_e32 v4, 1, v1
	s_nop 1
	v_cndmask_b32_e32 v1, v1, v4, vcc
	v_add_u32_e32 v1, 1, v1
	v_add_u32_e32 v4, 1, v3
	v_mul_lo_u32 v7, v1, v2
	v_mul_lo_u32 v13, v1, v12
	v_cmp_ne_u32_e32 vcc, v4, v7
	s_nop 1
	s_cbranch_vccnz .Lxb4_wait
	buffer_wbl2 sc1
	s_waitcnt vmcnt(0)
	global_atomic_add v[10:11], v6, off

; template <class T> __device__ __forceinline__ T* opaque_p(T* p) { asm volatile("" : "+s"(p)); return p; }
; __device__ __forceinline__ int tidx(int wid) { int l; asm volatile("v_mbcnt_lo_u32_b32 %0, -1, 0\n\tv_mbcnt_hi_u32_b32 %0, -1, %0" : "=v"(l)); return (wid << 6) + l; }
; __device__ __forceinline__ unsigned xb_add(unsigned* p, unsigned v) { return __hip_atomic_fetch_add(p, v, __ATOMIC_RELAXED, __HIP_MEMORY_SCOPE_AGENT); }
; __device__ __forceinline__ void xcd_barrier(const XcdBarrier& b, int wid0) {
;     asm volatile("s_waitcnt vmcnt(0)" ::: "memory");
;     __syncthreads();
;     if (tidx(wid0) == 0) {
;         unsigned* bar = opaque_p(b.bar);
;         __builtin_amdgcn_s_waitcnt(0);
;         unsigned nloc = b.st[0], nx = b.st[1];
;         if (nloc == 0u) { xcd_barrier_complete(bar, b.x, nloc, nx); b.st[0] = nloc; b.st[1] = nx; }
;         const unsigned old = xb_add(&bar[XB_XSUB(b.x)], 1u);
;         const unsigned gen = old / nloc;
;         if (old + 1u == (gen + 1u) * nloc) {
;             __builtin_amdgcn_fence(__ATOMIC_RELEASE, "agent");
;             asm volatile("s_waitcnt vmcnt(0)" ::: "memory");
;             const unsigned og = xb_add(&bar[XB_TOP], 1u);
;             const unsigned tg = og / nx;
;             if (og + 1u == (tg + 1u) * nx) xb_add(&bar[XB_TOPGEN], 1u);
.LBB0_934:
	s_add_i32 s0, s77, 8
	s_cmp_lt_i32 s0, s61
	s_cselect_b64 s[0:1], -1, 0
	s_and_b64 s[0:1], s[20:21], s[0:1]
	s_andn2_b64 vcc, exec, s[0:1]
	s_cbranch_vccnz .LBB0_980
	s_waitcnt vmcnt(0)
	s_waitcnt vmcnt(0) lgkmcnt(0)
	s_barrier
	v_mbcnt_lo_u32_b32 v0, -1, 0
	v_mbcnt_hi_u32_b32 v0, -1, v0
	s_nop 0
	v_cmp_eq_u32_e32 vcc, s86, v0
	s_and_saveexec_b64 s[30:31], vcc
	s_cbranch_execz .LBB0_979
	v_readlane_b32 s34, v255, 3
	v_readlane_b32 s0, v255, 17
	v_readlane_b32 s35, v255, 4
	v_readlane_b32 s1, v255, 18
	s_lshl_b32 s2, s91, 2
	s_add_u32 s2, s34, s2
	s_addc_u32 s3, s35, 0
	s_add_u32 s4, s2, 0x1400
	s_addc_u32 s5, s3, 0
	s_add_u32 s6, s34, 0x3400
	s_addc_u32 s7, s35, 0
	v_mov_b32_e32 v0, s0
	v_mov_b32_e32 v1, s1
	ds_read_b32 v2, v0
	ds_read_b32 v12, v1
	v_mov_b32_e32 v6, 1
	v_mov_b32_e32 v8, s4
	v_mov_b32_e32 v9, s5
	s_add_u32 s10, s2, 0x2400
	s_addc_u32 s11, s3, 0
	v_mov_b32_e32 v16, s10
	v_mov_b32_e32 v17, s11
	v_mov_b32_e32 v10, s6
	v_mov_b32_e32 v11, s7
	s_nop 0
	global_atomic_add v3, v[8:9], v6, off sc0
	s_waitcnt lgkmcnt(0)
	v_cvt_f32_u32_e32 v1, v2
	v_sub_u32_e32 v4, 0, v2
	v_rcp_iflag_f32_e32 v1, v1
	s_nop 0
	v_mul_f32_e32 v1, 0x4f7ffffe, v1
	v_cvt_u32_f32_e32 v1, v1
	v_mul_lo_u32 v4, v4, v1
	v_mul_hi_u32 v4, v1, v4
	v_add_u32_e32 v1, v1, v4
	s_mov_b32 s8, 0
	s_waitcnt vmcnt(0)
	v_mul_hi_u32 v1, v3, v1
	v_mul_lo_u32 v4, v1, v2
	v_sub_u32_e32 v4, v3, v4
	v_cmp_ge_u32_e32 vcc, v4, v2
	v_add_u32_e32 v5, 1, v1
	s_nop 1
	v_cndmask_b32_e32 v1, v1, v5, vcc
	v_sub_u32_e32 v5, v4, v2
	v_cndmask_b32_e32 v4, v4, v5, vcc
	v_cmp_ge_u32_e32 vcc, v4, v2
	v_add_u32_e32 v4, 1, v1
	s_nop 1
	v_cndmask_b32_e32 v1, v1, v4, vcc
	v_add_u32_e32 v1, 1, v1
	v_add_u32_e32 v4, 1, v3
	v_mul_lo_u32 v7, v1, v2
	v_mul_lo_u32 v13, v1, v12
	v_cmp_ne_u32_e32 vcc, v4, v7
	s_nop 1
	s_cbranch_vccnz .Lxb5_wait
	buffer_wbl2 sc1
	s_waitcnt vmcnt(0)
	global_atomic_add v[10:11], v6, off

; template <class T> __device__ __forceinline__ T* opaque_p(T* p) { asm volatile("" : "+s"(p)); return p; }
; __device__ __forceinline__ int tidx(int wid) { int l; asm volatile("v_mbcnt_lo_u32_b32 %0, -1, 0\n\tv_mbcnt_hi_u32_b32 %0, -1, %0" : "=v"(l)); return (wid << 6) + l; }
; __device__ __forceinline__ unsigned xb_add(unsigned* p, unsigned v) { return __hip_atomic_fetch_add(p, v, __ATOMIC_RELAXED, __HIP_MEMORY_SCOPE_AGENT); }
; __device__ __forceinline__ void xcd_barrier(const XcdBarrier& b, int wid0) {
;     asm volatile("s_waitcnt vmcnt(0)" ::: "memory");
;     __syncthreads();
;     if (tidx(wid0) == 0) {
;         unsigned* bar = opaque_p(b.bar);
;         __builtin_amdgcn_s_waitcnt(0);
;         unsigned nloc = b.st[0], nx = b.st[1];
;         if (nloc == 0u) { xcd_barrier_complete(bar, b.x, nloc, nx); b.st[0] = nloc; b.st[1] = nx; }
;         const unsigned old = xb_add(&bar[XB_XSUB(b.x)], 1u);
;         const unsigned gen = old / nloc;
;         if (old + 1u == (gen + 1u) * nloc) {
;             __builtin_amdgcn_fence(__ATOMIC_RELEASE, "agent");
;             asm volatile("s_waitcnt vmcnt(0)" ::: "memory");
;             const unsigned og = xb_add(&bar[XB_TOP], 1u);
;             const unsigned tg = og / nx;
;             if (og + 1u == (tg + 1u) * nx) xb_add(&bar[XB_TOPGEN], 1u);
.LBB0_1033:
	s_waitcnt vmcnt(0)
	s_waitcnt vmcnt(0) lgkmcnt(0)
	s_barrier
	v_mbcnt_lo_u32_b32 v0, -1, 0
	v_mbcnt_hi_u32_b32 v0, -1, v0
	s_nop 0
	v_cmp_eq_u32_e32 vcc, s86, v0
	s_and_saveexec_b64 s[30:31], vcc
	s_cbranch_execz .LBB0_1077
	v_readlane_b32 s34, v255, 3
	v_readlane_b32 s0, v255, 17
	v_readlane_b32 s35, v255, 4
	v_readlane_b32 s1, v255, 18
	s_lshl_b32 s2, s91, 2
	s_add_u32 s2, s34, s2
	s_addc_u32 s3, s35, 0
	s_add_u32 s4, s2, 0x1400
	s_addc_u32 s5, s3, 0
	s_add_u32 s6, s34, 0x3400
	s_addc_u32 s7, s35, 0
	v_mov_b32_e32 v0, s0
	v_mov_b32_e32 v1, s1
	ds_read_b32 v2, v0
	ds_read_b32 v12, v1
	v_mov_b32_e32 v6, 1
	v_mov_b32_e32 v8, s4
	v_mov_b32_e32 v9, s5
	s_add_u32 s10, s2, 0x2400
	s_addc_u32 s11, s3, 0
	v_mov_b32_e32 v16, s10
	v_mov_b32_e32 v17, s11
	v_mov_b32_e32 v10, s6
	v_mov_b32_e32 v11, s7
	s_nop 0
	global_atomic_add v3, v[8:9], v6, off sc0
	s_waitcnt lgkmcnt(0)
	v_cvt_f32_u32_e32 v1, v2
	v_sub_u32_e32 v4, 0, v2
	v_rcp_iflag_f32_e32 v1, v1
	s_nop 0
	v_mul_f32_e32 v1, 0x4f7ffffe, v1
	v_cvt_u32_f32_e32 v1, v1
	v_mul_lo_u32 v4, v4, v1
	v_mul_hi_u32 v4, v1, v4
	v_add_u32_e32 v1, v1, v4
	s_mov_b32 s8, 0
	s_waitcnt vmcnt(0)
	v_mul_hi_u32 v1, v3, v1
	v_mul_lo_u32 v4, v1, v2
	v_sub_u32_e32 v4, v3, v4
	v_cmp_ge_u32_e32 vcc, v4, v2
	v_add_u32_e32 v5, 1, v1
	s_nop 1
	v_cndmask_b32_e32 v1, v1, v5, vcc
	v_sub_u32_e32 v5, v4, v2
	v_cndmask_b32_e32 v4, v4, v5, vcc
	v_cmp_ge_u32_e32 vcc, v4, v2
	v_add_u32_e32 v4, 1, v1
	s_nop 1
	v_cndmask_b32_e32 v1, v1, v4, vcc
	v_add_u32_e32 v1, 1, v1
	v_add_u32_e32 v4, 1, v3
	v_mul_lo_u32 v7, v1, v2
	v_mul_lo_u32 v13, v1, v12
	v_cmp_ne_u32_e32 vcc, v4, v7
	s_nop 1
	s_cbranch_vccnz .Lxb6_wait
	buffer_wbl2 sc1
	s_waitcnt vmcnt(0)
	global_atomic_add v[10:11], v6, off

; template <class T> __device__ __forceinline__ T* opaque_p(T* p) { asm volatile("" : "+s"(p)); return p; }
; __device__ __forceinline__ int tidx(int wid) { int l; asm volatile("v_mbcnt_lo_u32_b32 %0, -1, 0\n\tv_mbcnt_hi_u32_b32 %0, -1, %0" : "=v"(l)); return (wid << 6) + l; }
; __device__ __forceinline__ unsigned xb_add(unsigned* p, unsigned v) { return __hip_atomic_fetch_add(p, v, __ATOMIC_RELAXED, __HIP_MEMORY_SCOPE_AGENT); }
; __device__ __forceinline__ void xcd_barrier(const XcdBarrier& b, int wid0) {
;     asm volatile("s_waitcnt vmcnt(0)" ::: "memory");
;     __syncthreads();
;     if (tidx(wid0) == 0) {
;         unsigned* bar = opaque_p(b.bar);
;         __builtin_amdgcn_s_waitcnt(0);
;         unsigned nloc = b.st[0], nx = b.st[1];
;         if (nloc == 0u) { xcd_barrier_complete(bar, b.x, nloc, nx); b.st[0] = nloc; b.st[1] = nx; }
;         const unsigned old = xb_add(&bar[XB_XSUB(b.x)], 1u);
;         const unsigned gen = old / nloc;
;         if (old + 1u == (gen + 1u) * nloc) {
;             __builtin_amdgcn_fence(__ATOMIC_RELEASE, "agent");
;             asm volatile("s_waitcnt vmcnt(0)" ::: "memory");
;             const unsigned og = xb_add(&bar[XB_TOP], 1u);
;             const unsigned tg = og / nx;
;             if (og + 1u == (tg + 1u) * nx) xb_add(&bar[XB_TOPGEN], 1u);
.LBB0_1145:
	s_add_i32 s36, s77, 11
	s_cmp_ge_i32 s36, s61
	s_cbranch_scc1 .LBB0_1191
	s_waitcnt vmcnt(0)
	s_waitcnt vmcnt(0) lgkmcnt(0)
	s_barrier
	v_mbcnt_lo_u32_b32 v0, -1, 0
	v_mbcnt_hi_u32_b32 v0, -1, v0
	s_nop 0
	v_cmp_eq_u32_e32 vcc, s86, v0
	s_and_saveexec_b64 s[30:31], vcc
	s_cbranch_execz .LBB0_1190
	v_readlane_b32 s34, v255, 3
	v_readlane_b32 s0, v255, 17
	v_readlane_b32 s35, v255, 4
	v_readlane_b32 s1, v255, 18
	s_lshl_b32 s2, s91, 2
	s_add_u32 s2, s34, s2
	s_addc_u32 s3, s35, 0
	s_add_u32 s4, s2, 0x1400
	s_addc_u32 s5, s3, 0
	s_add_u32 s6, s34, 0x3400
	s_addc_u32 s7, s35, 0
	v_mov_b32_e32 v0, s0
	v_mov_b32_e32 v1, s1
	ds_read_b32 v2, v0
	ds_read_b32 v12, v1
	v_mov_b32_e32 v6, 1
	v_mov_b32_e32 v8, s4
	v_mov_b32_e32 v9, s5
	s_add_u32 s10, s2, 0x2400
	s_addc_u32 s11, s3, 0
	v_mov_b32_e32 v16, s10
	v_mov_b32_e32 v17, s11
	v_mov_b32_e32 v10, s6
	v_mov_b32_e32 v11, s7
	s_nop 0
	global_atomic_add v3, v[8:9], v6, off sc0
	s_waitcnt lgkmcnt(0)
	v_cvt_f32_u32_e32 v1, v2
	v_sub_u32_e32 v4, 0, v2
	v_rcp_iflag_f32_e32 v1, v1
	s_nop 0
	v_mul_f32_e32 v1, 0x4f7ffffe, v1
	v_cvt_u32_f32_e32 v1, v1
	v_mul_lo_u32 v4, v4, v1
	v_mul_hi_u32 v4, v1, v4
	v_add_u32_e32 v1, v1, v4
	s_mov_b32 s8, 0
	s_waitcnt vmcnt(0)
	v_mul_hi_u32 v1, v3, v1
	v_mul_lo_u32 v4, v1, v2
	v_sub_u32_e32 v4, v3, v4
	v_cmp_ge_u32_e32 vcc, v4, v2
	v_add_u32_e32 v5, 1, v1
	s_nop 1
	v_cndmask_b32_e32 v1, v1, v5, vcc
	v_sub_u32_e32 v5, v4, v2
	v_cndmask_b32_e32 v4, v4, v5, vcc
	v_cmp_ge_u32_e32 vcc, v4, v2
	v_add_u32_e32 v4, 1, v1
	s_nop 1
	v_cndmask_b32_e32 v1, v1, v4, vcc
	v_add_u32_e32 v1, 1, v1
	v_add_u32_e32 v4, 1, v3
	v_mul_lo_u32 v7, v1, v2
	v_mul_lo_u32 v13, v1, v12
	v_cmp_ne_u32_e32 vcc, v4, v7
	s_nop 1
	s_cbranch_vccnz .Lxb7_wait
	buffer_wbl2 sc1
	s_waitcnt vmcnt(0)
	global_atomic_add v[10:11], v6, off

; template <class T> __device__ __forceinline__ T* opaque_p(T* p) { asm volatile("" : "+s"(p)); return p; }
; __device__ __forceinline__ int tidx(int wid) { int l; asm volatile("v_mbcnt_lo_u32_b32 %0, -1, 0\n\tv_mbcnt_hi_u32_b32 %0, -1, %0" : "=v"(l)); return (wid << 6) + l; }
; __device__ __forceinline__ unsigned xb_add(unsigned* p, unsigned v) { return __hip_atomic_fetch_add(p, v, __ATOMIC_RELAXED, __HIP_MEMORY_SCOPE_AGENT); }
; __device__ __forceinline__ void xcd_barrier(const XcdBarrier& b, int wid0) {
;     asm volatile("s_waitcnt vmcnt(0)" ::: "memory");
;     __syncthreads();
;     if (tidx(wid0) == 0) {
;         unsigned* bar = opaque_p(b.bar);
;         __builtin_amdgcn_s_waitcnt(0);
;         unsigned nloc = b.st[0], nx = b.st[1];
;         if (nloc == 0u) { xcd_barrier_complete(bar, b.x, nloc, nx); b.st[0] = nloc; b.st[1] = nx; }
;         const unsigned old = xb_add(&bar[XB_XSUB(b.x)], 1u);
;         const unsigned gen = old / nloc;
;         if (old + 1u == (gen + 1u) * nloc) {
;             __builtin_amdgcn_fence(__ATOMIC_RELEASE, "agent");
;             asm volatile("s_waitcnt vmcnt(0)" ::: "memory");
;             const unsigned og = xb_add(&bar[XB_TOP], 1u);
;             const unsigned tg = og / nx;
;             if (og + 1u == (tg + 1u) * nx) xb_add(&bar[XB_TOPGEN], 1u);
.LBB0_1284:
	s_add_i32 s36, s77, 12
	s_cmp_ge_i32 s36, s61
	s_cbranch_scc1 .LBB0_1330
	s_waitcnt vmcnt(0)
	s_waitcnt lgkmcnt(0)
	s_barrier
	s_waitcnt vmcnt(0)
	v_mbcnt_lo_u32_b32 v0, -1, 0
	v_mbcnt_hi_u32_b32 v0, -1, v0
	s_nop 0
	v_cmp_eq_u32_e32 vcc, s86, v0
	s_and_saveexec_b64 s[30:31], vcc
	s_cbranch_execz .LBB0_1329
	v_readlane_b32 s34, v255, 3
	v_readlane_b32 s0, v255, 17
	v_readlane_b32 s35, v255, 4
	v_readlane_b32 s1, v255, 18
	s_lshl_b32 s2, s91, 2
	s_add_u32 s2, s34, s2
	s_addc_u32 s3, s35, 0
	s_add_u32 s4, s2, 0x1400
	s_addc_u32 s5, s3, 0
	s_add_u32 s6, s34, 0x3400
	s_addc_u32 s7, s35, 0
	v_mov_b32_e32 v0, s0
	v_mov_b32_e32 v1, s1
	ds_read_b32 v2, v0
	ds_read_b32 v12, v1
	v_mov_b32_e32 v6, 1
	v_mov_b32_e32 v8, s4
	v_mov_b32_e32 v9, s5
	s_add_u32 s10, s2, 0x2400
	s_addc_u32 s11, s3, 0
	v_mov_b32_e32 v16, s10
	v_mov_b32_e32 v17, s11
	v_mov_b32_e32 v10, s6
	v_mov_b32_e32 v11, s7
	s_nop 0
	global_atomic_add v3, v[8:9], v6, off sc0
	s_waitcnt lgkmcnt(0)
	v_cvt_f32_u32_e32 v1, v2
	v_sub_u32_e32 v4, 0, v2
	v_rcp_iflag_f32_e32 v1, v1
	s_nop 0
	v_mul_f32_e32 v1, 0x4f7ffffe, v1
	v_cvt_u32_f32_e32 v1, v1
	v_mul_lo_u32 v4, v4, v1
	v_mul_hi_u32 v4, v1, v4
	v_add_u32_e32 v1, v1, v4
	s_mov_b32 s8, 0
	s_waitcnt vmcnt(0)
	v_mul_hi_u32 v1, v3, v1
	v_mul_lo_u32 v4, v1, v2
	v_sub_u32_e32 v4, v3, v4
	v_cmp_ge_u32_e32 vcc, v4, v2
	v_add_u32_e32 v5, 1, v1
	s_nop 1
	v_cndmask_b32_e32 v1, v1, v5, vcc
	v_sub_u32_e32 v5, v4, v2
	v_cndmask_b32_e32 v4, v4, v5, vcc
	v_cmp_ge_u32_e32 vcc, v4, v2
	v_add_u32_e32 v4, 1, v1
	s_nop 1
	v_cndmask_b32_e32 v1, v1, v4, vcc
	v_add_u32_e32 v1, 1, v1
	v_add_u32_e32 v4, 1, v3
	v_mul_lo_u32 v7, v1, v2
	v_mul_lo_u32 v13, v1, v12
	v_cmp_ne_u32_e32 vcc, v4, v7
	s_nop 1
	s_cbranch_vccnz .Lxb8_wait
	buffer_wbl2 sc1
	s_waitcnt vmcnt(0)
	global_atomic_add v[10:11], v6, off

; template <class T> __device__ __forceinline__ T* opaque_p(T* p) { asm volatile("" : "+s"(p)); return p; }
; __device__ __forceinline__ int tidx(int wid) { int l; asm volatile("v_mbcnt_lo_u32_b32 %0, -1, 0\n\tv_mbcnt_hi_u32_b32 %0, -1, %0" : "=v"(l)); return (wid << 6) + l; }
; __device__ __forceinline__ unsigned xb_add(unsigned* p, unsigned v) { return __hip_atomic_fetch_add(p, v, __ATOMIC_RELAXED, __HIP_MEMORY_SCOPE_AGENT); }
; __device__ __forceinline__ void xcd_barrier(const XcdBarrier& b, int wid0) {
;     asm volatile("s_waitcnt vmcnt(0)" ::: "memory");
;     __syncthreads();
;     if (tidx(wid0) == 0) {
;         unsigned* bar = opaque_p(b.bar);
;         __builtin_amdgcn_s_waitcnt(0);
;         unsigned nloc = b.st[0], nx = b.st[1];
;         if (nloc == 0u) { xcd_barrier_complete(bar, b.x, nloc, nx); b.st[0] = nloc; b.st[1] = nx; }
;         const unsigned old = xb_add(&bar[XB_XSUB(b.x)], 1u);
;         const unsigned gen = old / nloc;
;         if (old + 1u == (gen + 1u) * nloc) {
;             __builtin_amdgcn_fence(__ATOMIC_RELEASE, "agent");
;             asm volatile("s_waitcnt vmcnt(0)" ::: "memory");
;             const unsigned og = xb_add(&bar[XB_TOP], 1u);
;             const unsigned tg = og / nx;
;             if (og + 1u == (tg + 1u) * nx) xb_add(&bar[XB_TOPGEN], 1u);
.LBB0_1507:
	v_readlane_b32 s34, v255, 3
	v_readlane_b32 s0, v255, 17
	v_readlane_b32 s35, v255, 4
	v_readlane_b32 s1, v255, 18
	s_lshl_b32 s2, s91, 2
	s_add_u32 s2, s34, s2
	s_addc_u32 s3, s35, 0
	s_add_u32 s4, s2, 0x1400
	s_addc_u32 s5, s3, 0
	s_add_u32 s6, s34, 0x3400
	s_addc_u32 s7, s35, 0
	v_mov_b32_e32 v0, s0
	v_mov_b32_e32 v1, s1
	ds_read_b32 v2, v0
	ds_read_b32 v12, v1
	v_mov_b32_e32 v6, 1
	v_mov_b32_e32 v8, s4
	v_mov_b32_e32 v9, s5
	s_add_u32 s10, s2, 0x2400
	s_addc_u32 s11, s3, 0
	v_mov_b32_e32 v16, s10
	v_mov_b32_e32 v17, s11
	v_mov_b32_e32 v10, s6
	v_mov_b32_e32 v11, s7
	s_nop 0
	global_atomic_add v3, v[8:9], v6, off sc0
	s_waitcnt lgkmcnt(0)
	v_cvt_f32_u32_e32 v1, v2
	v_sub_u32_e32 v4, 0, v2
	v_rcp_iflag_f32_e32 v1, v1
	s_nop 0
	v_mul_f32_e32 v1, 0x4f7ffffe, v1
	v_cvt_u32_f32_e32 v1, v1
	v_mul_lo_u32 v4, v4, v1
	v_mul_hi_u32 v4, v1, v4
	v_add_u32_e32 v1, v1, v4
	s_mov_b32 s8, 0
	s_waitcnt vmcnt(0)
	v_mul_hi_u32 v1, v3, v1
	v_mul_lo_u32 v4, v1, v2
	v_sub_u32_e32 v4, v3, v4
	v_cmp_ge_u32_e32 vcc, v4, v2
	v_add_u32_e32 v5, 1, v1
	s_nop 1
	v_cndmask_b32_e32 v1, v1, v5, vcc
	v_sub_u32_e32 v5, v4, v2
	v_cndmask_b32_e32 v4, v4, v5, vcc
	v_cmp_ge_u32_e32 vcc, v4, v2
	v_add_u32_e32 v4, 1, v1
	s_nop 1
	v_cndmask_b32_e32 v1, v1, v4, vcc
	v_add_u32_e32 v1, 1, v1
	v_add_u32_e32 v4, 1, v3
	v_mul_lo_u32 v7, v1, v2
	v_mul_lo_u32 v13, v1, v12
	v_cmp_ne_u32_e32 vcc, v4, v7
	s_nop 1
	s_cbranch_vccnz .Lxb9_wait
	buffer_wbl2 sc1
	s_waitcnt vmcnt(0)
	global_atomic_add v[10:11], v6, off

; __device__ __forceinline__ unsigned xb_ld(unsigned* p)              { return __hip_atomic_load(p, __ATOMIC_RELAXED, __HIP_MEMORY_SCOPE_AGENT); }
; #define XB_SPIN(cond, bar) do { unsigned _sp = 0; while (cond) { __builtin_amdgcn_s_sleep(1); \
;     if ((++_sp & 255u) == 0u) { if (xb_ld(&(bar)[XB_TMO])) break; if (_sp > XB_SPIN_CAP) { atomicAdd(&(bar)[XB_TMO], 1u); break; } } } } while (0)
; __device__ __forceinline__ void xcd_barrier(const XcdBarrier& b, int wid0) {
;     ...
;             XB_SPIN(xb_ld(&bar[XB_XGEN(b.x)]) == gen, bar);
;             __builtin_amdgcn_fence(__ATOMIC_ACQUIRE, "agent");
;             asm volatile("s_waitcnt vmcnt(0)" ::: "memory");
;         }
;     }
;     __syncthreads();
.Lxb9_done:
	s_branch .Lxb9_out
.LBB0_1531:
	s_mov_b64 s[10:11], 0x800
	s_mov_b32 s23, 0x42800000
